# baseline (speedup 1.0000x reference)
.LBB1_15:
	s_or_b64 exec, exec, s[12:13]
	v_and_b32_e32 v114, 31, v0
	s_mul_i32 s9, s67, 0x60
	s_cmp_lg_u32 s67, 0
	s_cselect_b64 s[74:75], -1, 0
	v_alignbit_b32 v126, v113, v112, 24
	v_cndmask_b32_e64 v126, v112, v126, s[74:75]
	v_bfe_u32 v91, v126, 0, 8
	v_mul_lo_u16_e32 v15, 0x4f, v91
	s_lshl_b32 s7, s66, 3
	v_lshrrev_b16_e32 v15, 9, v15
	s_or_b32 s8, s7, 0xb600
	v_and_b32_e32 v15, 62, v15
	v_add_u32_e32 v15, v91, v15
	s_movk_i32 s6, 0x48
	v_mov_b32_e32 v99, s8
	v_mad_u32_u24 v42, v15, s6, v99
	v_mad_u32_u24 v43, v115, s6, v42
	s_waitcnt lgkmcnt(0)
	s_barrier
	ds_read_b64 v[34:35], v43
	ds_read_b64 v[36:37], v43 offset:8
	ds_read_b64 v[38:39], v43 offset:1080
	ds_read_b64 v[40:41], v43 offset:1088
	v_mov_b32_e32 v2, v46
	v_mov_b32_e32 v3, v46
	v_mov_b32_e32 v4, v46
	v_mov_b32_e32 v5, v46
	v_mov_b32_e32 v6, v47
	v_mov_b32_e32 v7, v47
	v_mov_b32_e32 v8, v47
	v_mov_b32_e32 v9, v47
	v_mov_b32_e32 v10, v48
	v_mov_b32_e32 v11, v48
	v_mov_b32_e32 v12, v48
	v_mov_b32_e32 v13, v48
	v_mov_b32_e32 v14, v49
	v_mov_b32_e32 v15, v49
	v_mov_b32_e32 v16, v49
	v_mov_b32_e32 v17, v49
	s_movk_i32 s8, 0x438
	s_add_i32 s12, s9, 32
	s_waitcnt lgkmcnt(2)
	v_mfma_f32_32x32x16_f16 v[18:33], v[86:89], v[34:37], v[2:17]
	v_add_u32_e32 v34, 0x8b8, v43
	ds_read_b64 v[36:37], v34 offset:8
	ds_read_b64 v[34:35], v34
	v_and_or_b32 v107, v0, 32, s7
	s_movk_i32 s7, 0x110
	v_mad_u32_u24 v91, v91, s7, v107
	s_add_i32 s9, s9, 64
	s_lshr_b32 s42, s3, 6
	s_waitcnt lgkmcnt(2)
	v_mfma_f32_32x32x16_f16 v[18:33], v[62:65], v[38:41], v[18:33]
	v_mad_u32_u24 v38, v115, s8, v42
	ds_read_b64 v[40:41], v38 offset:152
	ds_read_b64 v[38:39], v38 offset:144
	s_cmpk_lt_u32 s3, 0x100
	s_cselect_b64 s[30:31], -1, 0
	s_add_i32 s13, s69, 0x600
	s_add_i32 s14, s69, 0x700
	v_lshlrev_b32_e32 v116, 4, v115
	s_waitcnt lgkmcnt(2)
	v_mfma_f32_32x32x16_f16 v[18:33], v[58:61], v[34:37], v[18:33]
	v_add_u32_e32 v34, 0x870, v43
	ds_read_b64 v[36:37], v34 offset:8
	ds_read_b64 v[34:35], v34
	s_movk_i32 s15, 0x1070
	s_movk_i32 s16, 0x1ba0
	s_movk_i32 s17, 0x1c20
	s_waitcnt lgkmcnt(2)
	v_mfma_f32_32x32x16_f16 v[18:33], v[54:57], v[38:41], v[18:33]
	v_bfe_u32 v101, v126, 8, 8
	v_mul_lo_u16_e32 v38, 0x4f, v101
	v_lshrrev_b16_e32 v38, 9, v38
	v_and_b32_e32 v38, 62, v38
	v_add_u32_e32 v38, v101, v38
	v_mad_u32_u24 v97, v38, s6, v99
	v_mad_u32_u24 v106, v115, s6, v97
	ds_read_b64 v[92:93], v106
	ds_read_b64 v[94:95], v106 offset:8
	v_add_u32_e32 v96, 0x8b8, v106
	ds_read_b64 v[102:103], v96
	ds_read_b64 v[104:105], v96 offset:8
	s_waitcnt lgkmcnt(4)
	v_mfma_f32_32x32x16_f16 v[18:33], v[50:53], v[34:37], v[18:33]
	s_add_i32 s12, s69, 0x500
	s_addk_i32 s69, 0x800
	s_cmpk_gt_u32 s3, 0xff
	s_cselect_b64 vcc, -1, 0
	s_waitcnt lgkmcnt(2)
	v_mfma_f32_32x32x16_f16 v[34:49], v[86:89], v[92:95], v[2:17]
	ds_read_b64 v[92:93], v106 offset:1080
	ds_read_b64 v[94:95], v106 offset:1088
	s_nop 4
	v_cvt_pk_f16_f32 v18, v18, v19
	v_pk_max_f16 v96, v18, 0
	v_mad_u32_u24 v18, v115, s8, v97
	v_cvt_pk_f16_f32 v22, v22, v23
	v_add_u32_e32 v23, 0x870, v106
	v_cvt_pk_f16_f32 v30, v30, v31
	s_waitcnt lgkmcnt(0)
	v_mfma_f32_32x32x16_f16 v[34:49], v[62:65], v[92:95], v[34:49]
	v_cvt_pk_f16_f32 v92, v20, v21
	ds_read_b64 v[20:21], v18 offset:152
	ds_read_b64 v[18:19], v18 offset:144
	v_pk_max_f16 v97, v92, 0
	ds_read_b64 v[92:93], v23
	ds_read_b64 v[94:95], v23 offset:8
	v_cvt_pk_f16_f32 v31, v32, v33
	v_mfma_f32_32x32x16_f16 v[34:49], v[58:61], v[102:105], v[34:49]
	v_or_b32_e32 v102, 64, v114
	s_waitcnt lgkmcnt(2)
	v_mfma_f32_32x32x16_f16 v[34:49], v[54:57], v[18:21], v[34:49]
	v_cvt_pk_f16_f32 v19, v24, v25
	v_pk_max_f16 v18, v22, 0
	v_pk_max_f16 v19, v19, 0
	ds_write2_b64 v91, v[96:97], v[18:19] offset1:8
	v_cvt_pk_f16_f32 v18, v26, v27
	v_pk_max_f16 v26, v18, 0
	v_cvt_pk_f16_f32 v22, v28, v29
	v_bfe_u32 v28, v126, 16, 8
	v_mul_lo_u16_e32 v18, 0x4f, v28
	v_lshrrev_b16_e32 v18, 9, v18
	v_and_b32_e32 v18, 62, v18
	v_add_u32_e32 v18, v28, v18
	v_mad_u32_u24 v29, v18, s6, v99
	s_waitcnt lgkmcnt(1)
	v_mfma_f32_32x32x16_f16 v[34:49], v[50:53], v[92:95], v[34:49]
	v_add_u32_e32 v94, s68, v100
	v_add_u32_e32 v94, s69, v94
	v_mov_b32_e32 v95, 0
	v_lshl_add_u64 v[94:95], v[94:95], 4, s[22:23]
	global_load_dwordx4 v[94:97], v[94:95], off
	v_mad_u32_u24 v92, v115, s6, v29
	ds_read_b64 v[18:19], v92
	ds_read_b64 v[20:21], v92 offset:8
	v_pk_max_f16 v27, v22, 0
	ds_read_b64 v[22:23], v92 offset:1080
	ds_read_b64 v[24:25], v92 offset:1088
	v_or_b32_e32 v99, 32, v114
	s_nop 6
	v_cvt_pk_f16_f32 v32, v40, v41
	s_waitcnt lgkmcnt(2)
	v_mfma_f32_32x32x16_f16 v[2:17], v[86:89], v[18:21], v[2:17]
	v_pk_max_f16 v18, v30, 0
	v_pk_max_f16 v19, v31, 0
	ds_write2_b64 v91, v[26:27], v[18:19] offset0:16 offset1:24
	v_cvt_pk_f16_f32 v18, v34, v35
	v_cvt_pk_f16_f32 v19, v36, v37
	v_pk_max_f16 v26, v18, 0
	v_add_u32_e32 v18, 0x8b8, v92
	s_waitcnt lgkmcnt(1)
	v_mfma_f32_32x32x16_f16 v[2:17], v[62:65], v[22:25], v[2:17]
	v_pk_max_f16 v27, v19, 0
	ds_read_b64 v[20:21], v18 offset:8
	ds_read_b64 v[18:19], v18
	v_mad_u32_u24 v22, v115, s8, v29
	ds_read_b64 v[24:25], v22 offset:152
	ds_read_b64 v[22:23], v22 offset:144
	v_cvt_pk_f16_f32 v31, v38, v39
	v_mad_u32_u24 v30, v101, s7, v107
	s_and_b64 s[8:9], vcc, exec
	s_waitcnt lgkmcnt(2)
	v_mfma_f32_32x32x16_f16 v[2:17], v[58:61], v[18:21], v[2:17]
	v_pk_max_f16 v18, v31, 0
	v_pk_max_f16 v19, v32, 0
	ds_write2_b64 v30, v[26:27], v[18:19] offset1:8
	v_cvt_pk_f16_f32 v18, v42, v43
	v_cvt_pk_f16_f32 v19, v44, v45
	v_pk_max_f16 v26, v18, 0
	v_add_u32_e32 v18, 0x870, v92
	s_waitcnt lgkmcnt(1)
	v_mfma_f32_32x32x16_f16 v[2:17], v[54:57], v[22:25], v[2:17]
	v_pk_max_f16 v27, v19, 0
	ds_read_b64 v[20:21], v18 offset:8
	ds_read_b64 v[18:19], v18
	v_cvt_pk_f16_f32 v22, v46, v47
	v_cvt_pk_f16_f32 v23, v48, v49
	v_pk_max_f16 v22, v22, 0
	v_pk_max_f16 v23, v23, 0
	ds_write2_b64 v30, v[26:27], v[22:23] offset0:16 offset1:24
	s_waitcnt lgkmcnt(1)
	v_mfma_f32_32x32x16_f16 v[2:17], v[50:53], v[18:21], v[2:17]
	v_mad_u32_u24 v18, v28, s7, v107
	v_lshl_or_b32 v42, s66, 5, v116
	s_cselect_b32 s8, 0xf60, 0
	s_movk_i32 s9, 0xff0
	s_cselect_b32 s9, s9, 0x80
	s_cselect_b32 s15, s15, 0x110
	s_cselect_b32 s16, s16, 0x190
	s_nop 4
	v_cvt_pk_f16_f32 v2, v2, v3
	v_cvt_pk_f16_f32 v3, v4, v5
	v_cvt_pk_f16_f32 v4, v6, v7
	v_cvt_pk_f16_f32 v5, v8, v9
	v_pk_max_f16 v2, v2, 0
	v_pk_max_f16 v3, v3, 0
	v_pk_max_f16 v4, v4, 0
	v_pk_max_f16 v5, v5, 0
	ds_write2_b64 v18, v[2:3], v[4:5] offset1:8
	v_cvt_pk_f16_f32 v2, v10, v11
	v_cvt_pk_f16_f32 v3, v12, v13
	v_cvt_pk_f16_f32 v4, v14, v15
	v_cvt_pk_f16_f32 v5, v16, v17
	v_pk_max_f16 v2, v2, 0
	v_pk_max_f16 v3, v3, 0
	v_pk_max_f16 v4, v4, 0
	v_pk_max_f16 v5, v5, 0
	ds_write2_b64 v18, v[2:3], v[4:5] offset0:16 offset1:24
	s_waitcnt vmcnt(0)
	v_bfe_u32 v2, v117, 0, 8
	v_mul_u32_u24_e32 v3, 0xbb, v2
	v_lshrrev_b32_e32 v3, 11, v3
	v_lshl_add_u32 v103, v3, 1, v2
	v_bfe_u32 v2, v117, 8, 8
	v_mul_u32_u24_e32 v3, 0xbb, v2
	v_lshrrev_b32_e32 v3, 11, v3
	v_lshl_add_u32 v106, v3, 1, v2
	v_mad_u32_u24 v90, v103, s7, v42
	v_mad_u32_u24 v91, v106, s7, v42
	v_add_u32_e32 v2, s8, v90
	v_add_u32_e32 v6, s8, v91
	s_waitcnt lgkmcnt(0)
	s_barrier
	ds_read_b128 v[2:5], v2
	ds_read_b128 v[6:9], v6
	s_waitcnt lgkmcnt(1)
	v_mfma_f32_32x32x16_f16 v[18:33], v[82:85], v[2:5], 0
	v_add_u32_e32 v34, s9, v90
	v_add_u32_e32 v38, s9, v91
	ds_read_b128 v[34:37], v34
	ds_read_b128 v[38:41], v38
	s_cselect_b32 s17, s17, 0x220
	v_or_b32_e32 v101, 0x60, v114
	s_waitcnt lgkmcnt(2)
	v_mfma_f32_32x32x16_f16 v[2:17], v[82:85], v[6:9], 0
	s_waitcnt lgkmcnt(1)
	v_mfma_f32_32x32x16_f16 v[18:33], v[74:77], v[34:37], v[18:33]
	v_add_u32_e32 v34, s15, v90
	ds_read_b128 v[34:37], v34
	s_waitcnt lgkmcnt(1)
	v_mfma_f32_32x32x16_f16 v[2:17], v[74:77], v[38:41], v[2:17]
	v_add_u32_e32 v38, s15, v91
	ds_read_b128 v[38:41], v38
	s_waitcnt lgkmcnt(1)
	v_mfma_f32_32x32x16_f16 v[18:33], v[78:81], v[34:37], v[18:33]
	v_add_u32_e32 v34, s16, v90
	ds_read_b128 v[34:37], v34
	s_waitcnt lgkmcnt(1)
	v_mfma_f32_32x32x16_f16 v[2:17], v[78:81], v[38:41], v[2:17]
	v_add_u32_e32 v38, s16, v91
	ds_read_b128 v[38:41], v38
	s_waitcnt lgkmcnt(1)
	v_mfma_f32_32x32x16_f16 v[18:33], v[70:73], v[34:37], v[18:33]
	v_bfe_u32 v43, v117, 16, 8
	v_mul_u32_u24_e32 v34, 0xbb, v43
	v_lshrrev_b32_e32 v104, 11, v34
	v_add_u32_e32 v34, s17, v90
	ds_read_b128 v[34:37], v34
	v_lshl_add_u32 v104, v104, 1, v43
	v_mad_u32_u24 v92, v104, s7, v42
	s_waitcnt lgkmcnt(1)
	v_mfma_f32_32x32x16_f16 v[2:17], v[70:73], v[38:41], v[2:17]
	v_add_u32_e32 v38, s17, v91
	ds_read_b128 v[38:41], v38
	s_waitcnt lgkmcnt(1)
	v_mfma_f32_32x32x16_f16 v[18:33], v[66:69], v[34:37], v[18:33]
	v_bfe_u32 v34, v117, 24, 8
	v_mul_u32_u24_e32 v35, 0xbb, v34
	v_lshrrev_b32_e32 v35, 11, v35
	v_lshl_add_u32 v105, v35, 1, v34
	v_mad_u32_u24 v93, v105, s7, v42
	s_waitcnt lgkmcnt(0)
	v_mfma_f32_32x32x16_f16 v[2:17], v[66:69], v[38:41], v[2:17]
	v_add_u32_e32 v34, s8, v92
	v_add_u32_e32 v38, s8, v93
	ds_read_b128 v[34:37], v34
	ds_read_b128 v[38:41], v38
	v_add_u32_e32 v86, s9, v93
	s_waitcnt lgkmcnt(1)
	v_mfma_f32_32x32x16_f16 v[50:65], v[82:85], v[34:37], 0
	ds_read_b128 v[86:89], v86
	s_waitcnt lgkmcnt(1)
	v_mfma_f32_32x32x16_f16 v[34:49], v[82:85], v[38:41], 0
	v_add_u32_e32 v82, s9, v92
	ds_read_b128 v[82:85], v82
	s_waitcnt lgkmcnt(0)
	v_mfma_f32_32x32x16_f16 v[50:65], v[74:77], v[82:85], v[50:65]
	v_add_u32_e32 v82, s15, v93
	ds_read_b128 v[82:85], v82
	v_mfma_f32_32x32x16_f16 v[34:49], v[74:77], v[86:89], v[34:49]
	v_add_u32_e32 v74, s15, v92
	ds_read_b128 v[74:77], v74
	s_waitcnt lgkmcnt(0)
	v_mfma_f32_32x32x16_f16 v[50:65], v[78:81], v[74:77], v[50:65]
	v_add_u32_e32 v74, s16, v92
	ds_read_b128 v[74:77], v74
	v_mfma_f32_32x32x16_f16 v[34:49], v[78:81], v[82:85], v[34:49]
	v_add_u32_e32 v78, s16, v93
	ds_read_b128 v[78:81], v78
	s_waitcnt lgkmcnt(1)
	v_mfma_f32_32x32x16_f16 v[50:65], v[70:73], v[74:77], v[50:65]
	v_add_u32_e32 v74, s17, v93
	ds_read_b128 v[74:77], v74
	s_waitcnt lgkmcnt(1)
	v_mfma_f32_32x32x16_f16 v[34:49], v[70:73], v[78:81], v[34:49]
	v_add_u32_e32 v70, s17, v92
	ds_read_b128 v[70:73], v70
	s_waitcnt lgkmcnt(0)
	v_mfma_f32_32x32x16_f16 v[50:65], v[66:69], v[70:73], v[50:65]
	v_mfma_f32_32x32x16_f16 v[34:49], v[66:69], v[74:77], v[34:49]
	s_movk_i32 s7, 0x1cb0
	s_cselect_b32 s7, s7, 0x2a0
	v_add_u32_e32 v74, s7, v90
	ds_read_b128 v[74:77], v74
	v_add_u32_e32 v78, s7, v91
	ds_read_b128 v[78:81], v78
	s_movk_i32 s12, 0x1d30
	s_cselect_b32 s12, s12, 0xdd0
	s_movk_i32 s8, 0x1dc0
	s_cselect_b32 s8, s8, 0xe50
	s_movk_i32 s9, 0x1e40
	s_cselect_b32 s9, s9, 0xee0
	s_waitcnt vmcnt(0) lgkmcnt(1)
	v_mfma_f32_32x32x16_f16 v[18:33], v[108:111], v[74:77], v[18:33]
	v_add_u32_e32 v82, s12, v91
	ds_read_b128 v[82:85], v82
	s_waitcnt lgkmcnt(1)
	v_mfma_f32_32x32x16_f16 v[2:17], v[108:111], v[78:81], v[2:17]
	v_add_u32_e32 v78, s12, v90
	ds_read_b128 v[78:81], v78
	s_waitcnt lgkmcnt(0)
	v_mfma_f32_32x32x16_f16 v[18:33], v[118:121], v[78:81], v[18:33]
	v_add_u32_e32 v86, s8, v91
	ds_read_b128 v[86:89], v86
	v_mfma_f32_32x32x16_f16 v[2:17], v[118:121], v[82:85], v[2:17]
	v_add_u32_e32 v82, s8, v90
	ds_read_b128 v[82:85], v82
	s_waitcnt lgkmcnt(0)
	v_mfma_f32_32x32x16_f16 v[18:33], v[122:125], v[82:85], v[18:33]
	v_add_u32_e32 v82, s9, v90
	ds_read_b128 v[82:85], v82
	v_mfma_f32_32x32x16_f16 v[2:17], v[122:125], v[86:89], v[2:17]
	v_add_u32_e32 v86, s9, v91
	ds_read_b128 v[86:89], v86
	s_waitcnt lgkmcnt(1)
	v_mfma_f32_32x32x16_f16 v[18:33], v[94:97], v[82:85], v[18:33]
	s_waitcnt lgkmcnt(0)
	v_mfma_f32_32x32x16_f16 v[2:17], v[94:97], v[86:89], v[2:17]
	v_add_u32_e32 v82, s7, v92
	v_add_u32_e32 v86, s7, v93
	ds_read_b128 v[82:85], v82
	ds_read_b128 v[86:89], v86
	s_waitcnt lgkmcnt(1)
	v_mfma_f32_32x32x16_f16 v[50:65], v[108:111], v[82:85], v[50:65]
	v_add_u32_e32 v82, s12, v93
	ds_read_b128 v[82:85], v82
	s_waitcnt lgkmcnt(1)
	v_mfma_f32_32x32x16_f16 v[34:49], v[108:111], v[86:89], v[34:49]
	v_add_u32_e32 v66, s12, v92
	ds_read_b128 v[66:69], v66
	s_waitcnt lgkmcnt(0)
	v_mfma_f32_32x32x16_f16 v[50:65], v[118:121], v[66:69], v[50:65]
	v_add_u32_e32 v66, s8, v92
	ds_read_b128 v[66:69], v66
	v_mfma_f32_32x32x16_f16 v[34:49], v[118:121], v[82:85], v[34:49]
	v_add_u32_e32 v70, s8, v93
	ds_read_b128 v[70:73], v70
	s_waitcnt lgkmcnt(1)
	v_mfma_f32_32x32x16_f16 v[50:65], v[122:125], v[66:69], v[50:65]
	v_add_u32_e32 v66, s9, v92
	ds_read_b128 v[66:69], v66
	s_waitcnt lgkmcnt(1)
	v_mfma_f32_32x32x16_f16 v[34:49], v[122:125], v[70:73], v[34:49]
	v_add_u32_e32 v70, s9, v93
	ds_read_b128 v[70:73], v70
	s_waitcnt lgkmcnt(1)
	v_mfma_f32_32x32x16_f16 v[50:65], v[94:97], v[66:69], v[50:65]
	s_waitcnt lgkmcnt(0)
	v_mfma_f32_32x32x16_f16 v[34:49], v[94:97], v[70:73], v[34:49]
	s_cmpk_gt_u32 s3, 0x17f
	s_barrier
	s_cbranch_scc1 .LBB1_17
	s_mul_hi_u32 s7, s42, 0x55555556
	s_mul_i32 s7, s7, 3
	s_sub_i32 s7, s42, s7
	s_lshl_b32 s7, s7, 3
	s_add_i32 s8, s7, 0xb600
	s_cmpk_gt_u32 s3, 0xbf
	s_cselect_b64 s[74:75], -1, 0
	s_movk_i32 s12, 0x438
	s_movk_i32 s13, 0xd0
	v_alignbit_b32 v99, v113, v112, 24
	v_cndmask_b32_e64 v99, v112, v99, s[74:75]
	v_add_u32_e32 v122, 0xf550, v98
	ds_read_b128 v[82:85], v98 offset:62800
	ds_read_b128 v[86:89], v98 offset:63824
	ds_read_b128 v[90:93], v98 offset:64848
	ds_read_b128 v[94:97], v122 offset:3072
	ds_read_b128 v[118:121], v122 offset:4096
	ds_read_b32 v107, v122 offset:5120
	ds_read_b32 v112, v122 offset:5124
	ds_read_b32 v113, v122 offset:5128
	ds_read_b32 v117, v122 offset:5132
	v_bfe_u32 v101, v99, 0, 8
	v_mul_lo_u16_e32 v102, 0x4f, v101
	v_lshrrev_b16_e32 v102, 9, v102
	v_and_b32_e32 v102, 62, v102
	v_add_u32_e32 v102, v101, v102
	v_mov_b32_e32 v123, s8
	v_mad_u32_u24 v102, v102, s6, v123
	v_mad_u32_u24 v123, v115, s6, v102
	v_mad_u32_u24 v102, v115, s12, v102
	v_mad_u32_u24 v122, v115, 24, s7
	v_mad_u32_u24 v101, v101, s13, v122
	ds_read_b64 v[108:109], v123 offset:32
	ds_read_b64 v[110:111], v123 offset:40
	ds_read_b64 v[124:125], v123 offset:1112
	ds_read_b64 v[126:127], v123 offset:1120
	v_add_u32_e32 v122, 0x8d8, v123
	s_waitcnt lgkmcnt(2)
	v_mfma_f32_32x32x16_f16 v[66:81], v[82:85], v[108:111], 0
	ds_read_b64 v[108:109], v122
	ds_read_b64 v[110:111], v122 offset:8
	v_add_u32_e32 v122, 0x890, v123
	s_waitcnt lgkmcnt(2)
	v_mfma_f32_32x32x16_f16 v[66:81], v[86:89], v[124:127], v[66:81]
	ds_read_b64 v[124:125], v102 offset:176
	ds_read_b64 v[126:127], v102 offset:184
	s_waitcnt lgkmcnt(2)
	v_mfma_f32_32x32x16_f16 v[66:81], v[90:93], v[108:111], v[66:81]
	ds_read_b64 v[108:109], v122
	ds_read_b64 v[110:111], v122 offset:8
	s_waitcnt lgkmcnt(2)
	v_mfma_f32_32x32x16_f16 v[66:81], v[94:97], v[124:127], v[66:81]
	s_waitcnt lgkmcnt(0)
	v_mfma_f32_32x32x16_f16 v[66:81], v[118:121], v[108:111], v[66:81]
	v_bfe_u32 v124, v99, 8, 8
	v_mul_lo_u16_e32 v126, 0x4f, v124
	v_lshrrev_b16_e32 v126, 9, v126
	v_and_b32_e32 v126, 62, v126
	v_add_u32_e32 v126, v124, v126
	v_mov_b32_e32 v123, s8
	v_mad_u32_u24 v126, v126, s6, v123
	v_mad_u32_u24 v123, v115, s6, v126
	v_mad_u32_u24 v102, v115, s12, v126
	ds_read_b64 v[108:109], v123 offset:32
	ds_read_b64 v[110:111], v123 offset:40
	ds_read_b64 v[124:125], v123 offset:1112
	ds_read_b64 v[126:127], v123 offset:1120
	v_pk_add_f32 v[66:67], v[66:67], v[106:107] op_sel:[0,1] op_sel_hi:[1,1]
	v_pk_add_f32 v[68:69], v[68:69], v[106:107] op_sel:[0,1] op_sel_hi:[1,1]
	v_pk_add_f32 v[70:71], v[70:71], v[112:113] op_sel_hi:[1,0]
	v_pk_add_f32 v[72:73], v[72:73], v[112:113] op_sel_hi:[1,0]
	v_pk_add_f32 v[74:75], v[74:75], v[112:113] op_sel:[0,1] op_sel_hi:[1,1]
	v_pk_add_f32 v[76:77], v[76:77], v[112:113] op_sel:[0,1] op_sel_hi:[1,1]
	v_pk_add_f32 v[78:79], v[78:79], v[116:117] op_sel:[0,1] op_sel_hi:[1,1]
	v_pk_add_f32 v[80:81], v[80:81], v[116:117] op_sel:[0,1] op_sel_hi:[1,1]
	v_cvt_pk_f16_f32 v66, v66, v67
	v_cvt_pk_f16_f32 v67, v68, v69
	v_cvt_pk_f16_f32 v68, v70, v71
	v_cvt_pk_f16_f32 v69, v72, v73
	v_cvt_pk_f16_f32 v70, v74, v75
	v_cvt_pk_f16_f32 v71, v76, v77
	v_cvt_pk_f16_f32 v72, v78, v79
	v_cvt_pk_f16_f32 v73, v80, v81
	v_pk_max_f16 v66, v66, 0
	v_pk_max_f16 v67, v67, 0
	v_pk_max_f16 v68, v68, 0
	v_pk_max_f16 v69, v69, 0
	v_pk_max_f16 v70, v70, 0
	v_pk_max_f16 v71, v71, 0
	v_pk_max_f16 v72, v72, 0
	v_pk_max_f16 v73, v73, 0
	ds_write2_b64 v101, v[66:67], v[68:69] offset1:6
	ds_write2_b64 v101, v[70:71], v[72:73] offset0:12 offset1:18
	v_bfe_u32 v101, v99, 8, 8
	v_mad_u32_u24 v122, v115, 24, s7
	v_mad_u32_u24 v101, v101, s13, v122
	v_add_u32_e32 v122, 0x8d8, v123
	s_waitcnt lgkmcnt(4)
	v_mfma_f32_32x32x16_f16 v[66:81], v[82:85], v[108:111], 0
	ds_read_b64 v[108:109], v122
	ds_read_b64 v[110:111], v122 offset:8
	v_add_u32_e32 v122, 0x890, v123
	s_waitcnt lgkmcnt(2)
	v_mfma_f32_32x32x16_f16 v[66:81], v[86:89], v[124:127], v[66:81]
	ds_read_b64 v[124:125], v102 offset:176
	ds_read_b64 v[126:127], v102 offset:184
	s_waitcnt lgkmcnt(2)
	v_mfma_f32_32x32x16_f16 v[66:81], v[90:93], v[108:111], v[66:81]
	ds_read_b64 v[108:109], v122
	ds_read_b64 v[110:111], v122 offset:8
	s_waitcnt lgkmcnt(2)
	v_mfma_f32_32x32x16_f16 v[66:81], v[94:97], v[124:127], v[66:81]
	s_waitcnt lgkmcnt(0)
	v_mfma_f32_32x32x16_f16 v[66:81], v[118:121], v[108:111], v[66:81]
	v_bfe_u32 v124, v99, 16, 8
	v_mul_lo_u16_e32 v126, 0x4f, v124
	v_lshrrev_b16_e32 v126, 9, v126
	v_and_b32_e32 v126, 62, v126
	v_add_u32_e32 v126, v124, v126
	v_mov_b32_e32 v123, s8
	v_mad_u32_u24 v126, v126, s6, v123
	v_mad_u32_u24 v123, v115, s6, v126
	v_mad_u32_u24 v102, v115, s12, v126
	ds_read_b64 v[108:109], v123 offset:32
	ds_read_b64 v[110:111], v123 offset:40
	ds_read_b64 v[124:125], v123 offset:1112
	ds_read_b64 v[126:127], v123 offset:1120
	v_pk_add_f32 v[66:67], v[66:67], v[106:107] op_sel:[0,1] op_sel_hi:[1,1]
	v_pk_add_f32 v[68:69], v[68:69], v[106:107] op_sel:[0,1] op_sel_hi:[1,1]
	v_pk_add_f32 v[70:71], v[70:71], v[112:113] op_sel_hi:[1,0]
	v_pk_add_f32 v[72:73], v[72:73], v[112:113] op_sel_hi:[1,0]
	v_pk_add_f32 v[74:75], v[74:75], v[112:113] op_sel:[0,1] op_sel_hi:[1,1]
	v_pk_add_f32 v[76:77], v[76:77], v[112:113] op_sel:[0,1] op_sel_hi:[1,1]
	v_pk_add_f32 v[78:79], v[78:79], v[116:117] op_sel:[0,1] op_sel_hi:[1,1]
	v_pk_add_f32 v[80:81], v[80:81], v[116:117] op_sel:[0,1] op_sel_hi:[1,1]
	v_cvt_pk_f16_f32 v66, v66, v67
	v_cvt_pk_f16_f32 v67, v68, v69
	v_cvt_pk_f16_f32 v68, v70, v71
	v_cvt_pk_f16_f32 v69, v72, v73
	v_cvt_pk_f16_f32 v70, v74, v75
	v_cvt_pk_f16_f32 v71, v76, v77
	v_cvt_pk_f16_f32 v72, v78, v79
	v_cvt_pk_f16_f32 v73, v80, v81
	v_pk_max_f16 v66, v66, 0
	v_pk_max_f16 v67, v67, 0
	v_pk_max_f16 v68, v68, 0
	v_pk_max_f16 v69, v69, 0
	v_pk_max_f16 v70, v70, 0
	v_pk_max_f16 v71, v71, 0
	v_pk_max_f16 v72, v72, 0
	v_pk_max_f16 v73, v73, 0
	ds_write2_b64 v101, v[66:67], v[68:69] offset1:6
	ds_write2_b64 v101, v[70:71], v[72:73] offset0:12 offset1:18
	v_bfe_u32 v101, v99, 16, 8
	v_mad_u32_u24 v122, v115, 24, s7
	v_mad_u32_u24 v101, v101, s13, v122
	v_add_u32_e32 v122, 0x8d8, v123
	s_waitcnt lgkmcnt(4)
	v_mfma_f32_32x32x16_f16 v[66:81], v[82:85], v[108:111], 0
	ds_read_b64 v[108:109], v122
	ds_read_b64 v[110:111], v122 offset:8
	v_add_u32_e32 v122, 0x890, v123
	s_waitcnt lgkmcnt(2)
	v_mfma_f32_32x32x16_f16 v[66:81], v[86:89], v[124:127], v[66:81]
	ds_read_b64 v[124:125], v102 offset:176
	ds_read_b64 v[126:127], v102 offset:184
	s_waitcnt lgkmcnt(2)
	v_mfma_f32_32x32x16_f16 v[66:81], v[90:93], v[108:111], v[66:81]
	ds_read_b64 v[108:109], v122
	ds_read_b64 v[110:111], v122 offset:8
	s_waitcnt lgkmcnt(2)
	v_mfma_f32_32x32x16_f16 v[66:81], v[94:97], v[124:127], v[66:81]
	s_waitcnt lgkmcnt(0)
	v_mfma_f32_32x32x16_f16 v[66:81], v[118:121], v[108:111], v[66:81]
	v_or_b32_e32 v99, 32, v114
	v_or_b32_e32 v102, 64, v114
	s_nop 9
	v_pk_add_f32 v[66:67], v[66:67], v[106:107] op_sel:[0,1] op_sel_hi:[1,1]
	v_pk_add_f32 v[68:69], v[68:69], v[106:107] op_sel:[0,1] op_sel_hi:[1,1]
	v_pk_add_f32 v[70:71], v[70:71], v[112:113] op_sel_hi:[1,0]
	v_pk_add_f32 v[72:73], v[72:73], v[112:113] op_sel_hi:[1,0]
	v_pk_add_f32 v[74:75], v[74:75], v[112:113] op_sel:[0,1] op_sel_hi:[1,1]
	v_pk_add_f32 v[76:77], v[76:77], v[112:113] op_sel:[0,1] op_sel_hi:[1,1]
	v_pk_add_f32 v[78:79], v[78:79], v[116:117] op_sel:[0,1] op_sel_hi:[1,1]
	v_pk_add_f32 v[80:81], v[80:81], v[116:117] op_sel:[0,1] op_sel_hi:[1,1]
	v_cvt_pk_f16_f32 v66, v66, v67
	v_cvt_pk_f16_f32 v67, v68, v69
	v_cvt_pk_f16_f32 v68, v70, v71
	v_cvt_pk_f16_f32 v69, v72, v73
	v_cvt_pk_f16_f32 v70, v74, v75
	v_cvt_pk_f16_f32 v71, v76, v77
	v_cvt_pk_f16_f32 v72, v78, v79
	v_cvt_pk_f16_f32 v73, v80, v81
	v_pk_max_f16 v66, v66, 0
	v_pk_max_f16 v67, v67, 0
	v_pk_max_f16 v68, v68, 0
	v_pk_max_f16 v69, v69, 0
	v_pk_max_f16 v70, v70, 0
	v_pk_max_f16 v71, v71, 0
	v_pk_max_f16 v72, v72, 0
	v_pk_max_f16 v73, v73, 0
	ds_write2_b64 v101, v[66:67], v[68:69] offset1:6
	ds_write2_b64 v101, v[70:71], v[72:73] offset0:12 offset1:18
	v_or_b32_e32 v101, 0x60, v114
